# combo12a + nt on the read-once f32 weight loads of the P0 transposes and expert-u conversion
# baseline (speedup 1.0000x reference)
.LBB0_29:
	s_mov_b32 s1, 0
	s_mov_b32 s2, 0
	s_cmpk_gt_i32 s68, 0xbff
	s_cbranch_scc1 .LBB0_36
	v_mbcnt_lo_u32_b32 v0, -1, s2
	v_mbcnt_hi_u32_b32 v40, -1, v0
	v_readlane_b32 s2, v254, 4
	s_add_u32 s4, s48, 0x8400000
	v_readlane_b32 s3, v254, 5
	v_add_u32_e32 v37, s2, v40
	s_mul_hi_i32 s2, s68, 0x2aaaaaab
	s_addc_u32 s5, s49, 0
	s_lshr_b32 s3, s2, 31
	s_ashr_i32 s2, s2, 5
	s_add_i32 s2, s2, s3
	s_mul_i32 s3, s2, 0xc0
	s_sub_i32 s3, s68, s3
	v_ashrrev_i32_e32 v36, 4, v37
	v_lshl_add_u32 v30, s2, 8, v36
	s_lshl_b32 s2, s3, 6
	s_ashr_i32 s3, s2, 31
	s_lshl_b64 s[2:3], s[2:3], 2
	s_add_u32 s2, s24, s2
	v_lshlrev_b32_e32 v0, 4, v40
	s_addc_u32 s3, s25, s3
	v_and_b32_e32 v32, 0xf0, v0
	v_mov_b32_e32 v33, 0
	v_lshl_add_u64 v[24:25], s[2:3], 0, v[32:33]
	s_mov_b32 s2, 0xc040
	v_mad_i64_i32 v[8:9], s[6:7], v30, s2, v[24:25]
	v_add_u32_e32 v0, 32, v30
	v_mad_i64_i32 v[10:11], s[6:7], v0, s2, v[24:25]
	global_load_dwordx4 v[0:3], v[8:9], off nt
	global_load_dwordx4 v[4:7], v[10:11], off nt
	v_add_u32_e32 v8, 64, v30
	v_mad_i64_i32 v[16:17], s[6:7], v8, s2, v[24:25]
	v_add_u32_e32 v8, 0x60, v30
	v_mad_i64_i32 v[18:19], s[6:7], v8, s2, v[24:25]
	global_load_dwordx4 v[8:11], v[16:17], off nt
	global_load_dwordx4 v[12:15], v[18:19], off nt
	v_add_u32_e32 v16, 0x80, v30
	v_mad_i64_i32 v[26:27], s[6:7], v16, s2, v[24:25]
	v_add_u32_e32 v16, 0xa0, v30
	v_mad_i64_i32 v[28:29], s[6:7], v16, s2, v[24:25]
	global_load_dwordx4 v[16:19], v[26:27], off nt
	global_load_dwordx4 v[20:23], v[28:29], off nt
	v_add_u32_e32 v26, 0xc0, v30
	v_mad_i64_i32 v[34:35], s[6:7], v26, s2, v[24:25]
	v_add_u32_e32 v26, 0xe0, v30
	v_mad_i64_i32 v[38:39], s[6:7], v26, s2, v[24:25]
	global_load_dwordx4 v[24:27], v[34:35], off nt
	global_load_dwordx4 v[28:31], v[38:39], off nt
	v_add_u32_e32 v39, 0, v32
	v_lshl_add_u64 v[34:35], s[24:25], 0, v[32:33]
	v_lshlrev_b32_e32 v32, 5, v40
	v_ashrrev_i32_e32 v37, 3, v37
	v_and_b32_e32 v32, 0xe0, v32
	s_movk_i32 s3, 0x104
	v_mul_u32_u24_e32 v38, 0x104, v32
	v_lshlrev_b32_e32 v40, 2, v37
	v_add3_u32 v38, 0, v38, v40
	v_mul_lo_u32 v40, v36, s3
	v_add_u32_e32 v39, v39, v40
	s_lshl_b32 s10, s68, 6
	s_lshl_b32 s3, s46, 6
	v_add_u32_e32 v40, 0x2080, v39
	v_add_u32_e32 v41, 0x2088, v39
	v_add_u32_e32 v42, 0x4100, v39
	v_add_u32_e32 v43, 0x4108, v39
	v_add_u32_e32 v44, 0x6180, v39
	v_add_u32_e32 v45, 0x6188, v39
	v_add_u32_e32 v46, 0x8200, v39
	v_add_u32_e32 v47, 0x8208, v39
	v_add_u32_e32 v48, 0xa280, v39
	v_add_u32_e32 v49, 0xa288, v39
	v_add_u32_e32 v50, 0xc300, v39
	v_add_u32_e32 v51, 0xc308, v39
	v_add_u32_e32 v52, 0xe380, v39
	s_mov_b32 s31, s68
	global_load_dword v200, v[34:35], off
	global_load_dword v200, v[34:35], off
	s_branch .LBB0_32

.LBB0_34:
	s_andn2_b64 vcc, exec, s[8:9]
	s_cbranch_vccnz .LBB0_31
	s_mul_hi_i32 s8, s11, 0x2aaaaaab
	s_lshr_b32 s9, s8, 31
	s_ashr_i32 s8, s8, 5
	s_add_i32 s8, s8, s9
	v_lshl_add_u32 v30, s8, 8, v36
	s_mulk_i32 s8, 0xd000
	s_add_i32 s30, s3, s10
	s_add_i32 s8, s30, s8
	s_ashr_i32 s9, s8, 31
	v_lshl_add_u64 v[24:25], s[8:9], 2, v[34:35]
	v_mad_i64_i32 v[8:9], s[8:9], v30, s2, v[24:25]
	v_add_u32_e32 v0, 32, v30
	v_mad_i64_i32 v[10:11], s[8:9], v0, s2, v[24:25]
	global_load_dwordx4 v[0:3], v[8:9], off nt
	global_load_dwordx4 v[4:7], v[10:11], off nt
	v_add_u32_e32 v8, 64, v30
	v_mad_i64_i32 v[16:17], s[8:9], v8, s2, v[24:25]
	v_add_u32_e32 v8, 0x60, v30
	v_mad_i64_i32 v[18:19], s[8:9], v8, s2, v[24:25]
	global_load_dwordx4 v[8:11], v[16:17], off nt
	global_load_dwordx4 v[12:15], v[18:19], off nt
	v_add_u32_e32 v16, 0x80, v30
	v_mad_i64_i32 v[26:27], s[8:9], v16, s2, v[24:25]
	v_add_u32_e32 v16, 0xa0, v30
	v_mad_i64_i32 v[28:29], s[8:9], v16, s2, v[24:25]
	global_load_dwordx4 v[16:19], v[26:27], off nt
	global_load_dwordx4 v[20:23], v[28:29], off nt
	v_add_u32_e32 v26, 0xc0, v30
	v_mad_i64_i32 v[54:55], s[8:9], v26, s2, v[24:25]
	v_add_u32_e32 v26, 0xe0, v30
	v_mad_i64_i32 v[56:57], s[8:9], v26, s2, v[24:25]
	global_load_dwordx4 v[24:27], v[54:55], off nt
	global_load_dwordx4 v[28:31], v[56:57], off nt
	s_branch .LBB0_31
.LBB0_36:
	s_cmpk_lt_i32 s68, 0x400
	s_cselect_b64 s[4:5], -1, 0
	s_cmpk_gt_i32 s68, 0x3ff
	s_cbranch_scc1 .LBB0_43
	s_add_u32 s6, s48, 0xe400000
	s_addc_u32 s7, s49, 0
	s_waitcnt vmcnt(9)
	v_mbcnt_lo_u32_b32 v0, -1, s1
	s_ashr_i32 s1, s68, 31
	s_lshr_b32 s1, s1, 26
	v_mbcnt_hi_u32_b32 v40, -1, v0
	v_readlane_b32 s2, v254, 4
	s_add_i32 s1, s68, s1
	v_readlane_b32 s3, v254, 5
	v_add_u32_e32 v37, s2, v40
	s_and_b32 s2, s1, 0x3ffffc0
	s_sub_i32 s2, s68, s2
	s_lshl_b32 s2, s2, 6
	s_lshl_b32 s1, s1, 2
	s_ashr_i32 s3, s2, 31
	v_ashrrev_i32_e32 v36, 4, v37
	s_and_b32 s1, s1, 0xffffff00
	s_lshl_b64 s[2:3], s[2:3], 2
	s_waitcnt vmcnt(3)
	v_add_u32_e32 v24, s1, v36
	s_add_u32 s2, s28, s2
	v_lshlrev_b32_e32 v0, 4, v40
	s_addc_u32 s3, s29, s3
	v_and_b32_e32 v32, 0xf0, v0
	v_mov_b32_e32 v33, 0
	v_ashrrev_i32_e32 v25, 31, v24
	v_lshl_add_u64 v[26:27], s[2:3], 0, v[32:33]
	v_lshlrev_b64 v[0:1], 14, v[24:25]
	v_lshl_add_u64 v[8:9], v[26:27], 0, v[0:1]
	v_add_u32_e32 v0, 32, v24
	v_ashrrev_i32_e32 v1, 31, v0
	v_lshlrev_b64 v[0:1], 14, v[0:1]
	v_lshl_add_u64 v[10:11], v[26:27], 0, v[0:1]
	global_load_dwordx4 v[0:3], v[8:9], off nt
	global_load_dwordx4 v[4:7], v[10:11], off nt
	v_add_u32_e32 v8, 64, v24
	v_ashrrev_i32_e32 v9, 31, v8
	v_lshlrev_b64 v[8:9], 14, v[8:9]
	v_lshl_add_u64 v[16:17], v[26:27], 0, v[8:9]
	v_add_u32_e32 v8, 0x60, v24
	v_ashrrev_i32_e32 v9, 31, v8
	v_lshlrev_b64 v[8:9], 14, v[8:9]
	v_lshl_add_u64 v[18:19], v[26:27], 0, v[8:9]
	global_load_dwordx4 v[8:11], v[16:17], off nt
	global_load_dwordx4 v[12:15], v[18:19], off nt
	v_add_u32_e32 v16, 0x80, v24
	v_ashrrev_i32_e32 v17, 31, v16
	v_lshlrev_b64 v[16:17], 14, v[16:17]
	s_waitcnt vmcnt(6)
	v_lshl_add_u64 v[28:29], v[26:27], 0, v[16:17]
	v_add_u32_e32 v16, 0xa0, v24
	v_ashrrev_i32_e32 v17, 31, v16
	v_lshlrev_b64 v[16:17], 14, v[16:17]
	v_lshl_add_u64 v[30:31], v[26:27], 0, v[16:17]
	global_load_dwordx4 v[16:19], v[28:29], off nt
	global_load_dwordx4 v[20:23], v[30:31], off nt
	v_add_u32_e32 v28, 0xc0, v24
	v_ashrrev_i32_e32 v29, 31, v28
	v_add_u32_e32 v24, 0xe0, v24
	v_lshlrev_b64 v[28:29], 14, v[28:29]
	v_ashrrev_i32_e32 v25, 31, v24
	v_lshl_add_u64 v[34:35], v[26:27], 0, v[28:29]
	v_lshlrev_b64 v[24:25], 14, v[24:25]
	v_lshl_add_u64 v[38:39], v[26:27], 0, v[24:25]
	global_load_dwordx4 v[24:27], v[34:35], off nt
	global_load_dwordx4 v[28:31], v[38:39], off nt
	v_add_u32_e32 v39, 0, v32
	v_lshl_add_u64 v[34:35], s[28:29], 0, v[32:33]
	v_lshlrev_b32_e32 v32, 5, v40
	v_ashrrev_i32_e32 v37, 3, v37
	v_and_b32_e32 v32, 0xe0, v32
	s_movk_i32 s1, 0x104
	v_mul_u32_u24_e32 v38, 0x104, v32
	v_lshlrev_b32_e32 v40, 2, v37
	v_add3_u32 v38, 0, v38, v40
	v_mul_lo_u32 v40, v36, s1
	s_lshl_b32 s2, s68, 6
	s_lshl_b32 s1, s46, 6
	v_add_u32_e32 v39, v39, v40
	s_mov_b32 s29, s68
	global_load_dword v200, v[34:35], off
	global_load_dword v200, v[34:35], off
	s_branch .LBB0_39

.LBB0_41:
	s_andn2_b64 vcc, exec, s[10:11]
	s_cbranch_vccnz .LBB0_38
	s_ashr_i32 s10, s3, 31
	s_lshr_b32 s10, s10, 26
	s_add_i32 s10, s3, s10
	s_ashr_i32 s10, s10, 6
	v_lshl_add_u32 v24, s10, 8, v36
	s_add_i32 s28, s1, s2
	s_lshl_b32 s10, s10, 12
	s_sub_i32 s10, s28, s10
	s_ashr_i32 s11, s10, 31
	v_ashrrev_i32_e32 v25, 31, v24
	v_lshl_add_u64 v[26:27], s[10:11], 2, v[34:35]
	v_lshlrev_b64 v[0:1], 14, v[24:25]
	v_lshl_add_u64 v[8:9], v[26:27], 0, v[0:1]
	v_add_u32_e32 v0, 32, v24
	v_ashrrev_i32_e32 v1, 31, v0
	v_lshlrev_b64 v[0:1], 14, v[0:1]
	v_lshl_add_u64 v[10:11], v[26:27], 0, v[0:1]
	global_load_dwordx4 v[0:3], v[8:9], off nt
	global_load_dwordx4 v[4:7], v[10:11], off nt
	v_add_u32_e32 v8, 64, v24
	v_ashrrev_i32_e32 v9, 31, v8
	v_lshlrev_b64 v[8:9], 14, v[8:9]
	v_lshl_add_u64 v[16:17], v[26:27], 0, v[8:9]
	v_add_u32_e32 v8, 0x60, v24
	v_ashrrev_i32_e32 v9, 31, v8
	v_lshlrev_b64 v[8:9], 14, v[8:9]
	v_lshl_add_u64 v[18:19], v[26:27], 0, v[8:9]
	global_load_dwordx4 v[8:11], v[16:17], off nt
	global_load_dwordx4 v[12:15], v[18:19], off nt
	v_add_u32_e32 v16, 0x80, v24
	v_ashrrev_i32_e32 v17, 31, v16
	v_lshlrev_b64 v[16:17], 14, v[16:17]
	v_lshl_add_u64 v[28:29], v[26:27], 0, v[16:17]
	v_add_u32_e32 v16, 0xa0, v24
	v_ashrrev_i32_e32 v17, 31, v16
	v_lshlrev_b64 v[16:17], 14, v[16:17]
	v_lshl_add_u64 v[30:31], v[26:27], 0, v[16:17]
	global_load_dwordx4 v[16:19], v[28:29], off nt
	global_load_dwordx4 v[20:23], v[30:31], off nt
	v_add_u32_e32 v28, 0xc0, v24
	v_ashrrev_i32_e32 v29, 31, v28
	v_add_u32_e32 v24, 0xe0, v24
	v_lshlrev_b64 v[28:29], 14, v[28:29]
	v_ashrrev_i32_e32 v25, 31, v24
	v_lshl_add_u64 v[40:41], v[26:27], 0, v[28:29]
	v_lshlrev_b64 v[24:25], 14, v[24:25]
	v_lshl_add_u64 v[42:43], v[26:27], 0, v[24:25]
	global_load_dwordx4 v[24:27], v[40:41], off nt
	global_load_dwordx4 v[28:31], v[42:43], off nt
	s_branch .LBB0_38
.LBB0_43:
	s_mov_b32 s1, 0
	s_mov_b32 s2, 0
	s_cmpk_gt_i32 s68, 0xfff
	s_cbranch_scc1 .LBB0_50
	s_waitcnt vmcnt(9)
	v_mbcnt_lo_u32_b32 v0, -1, s2
	s_add_u32 s6, s48, 0x19400000
	v_mbcnt_hi_u32_b32 v40, -1, v0
	v_readlane_b32 s2, v254, 4
	s_addc_u32 s7, s49, 0
	v_readlane_b32 s3, v254, 5
	v_add_u32_e32 v37, s2, v40
	s_ashr_i32 s2, s68, 31
	s_lshr_b32 s2, s2, 26
	s_add_i32 s2, s68, s2
	s_and_b32 s3, s2, 0x3ffffc0
	s_lshl_b32 s2, s2, 2
	s_sub_i32 s3, s68, s3
	v_ashrrev_i32_e32 v36, 4, v37
	s_and_b32 s2, s2, 0xffffff00
	s_waitcnt vmcnt(3)
	v_add_u32_e32 v24, s2, v36
	s_lshl_b32 s2, s3, 6
	s_ashr_i32 s3, s2, 31
	s_lshl_b64 s[2:3], s[2:3], 2
	s_add_u32 s2, s26, s2
	v_lshlrev_b32_e32 v0, 4, v40
	s_addc_u32 s3, s27, s3
	v_and_b32_e32 v32, 0xf0, v0
	v_mov_b32_e32 v33, 0
	v_ashrrev_i32_e32 v25, 31, v24
	v_lshl_add_u64 v[26:27], s[2:3], 0, v[32:33]
	v_lshlrev_b64 v[0:1], 14, v[24:25]
	v_lshl_add_u64 v[8:9], v[26:27], 0, v[0:1]
	v_add_u32_e32 v0, 32, v24
	v_ashrrev_i32_e32 v1, 31, v0
	v_lshlrev_b64 v[0:1], 14, v[0:1]
	v_lshl_add_u64 v[10:11], v[26:27], 0, v[0:1]
	global_load_dwordx4 v[0:3], v[8:9], off nt
	global_load_dwordx4 v[4:7], v[10:11], off nt
	v_add_u32_e32 v8, 64, v24
	v_ashrrev_i32_e32 v9, 31, v8
	v_lshlrev_b64 v[8:9], 14, v[8:9]
	v_lshl_add_u64 v[16:17], v[26:27], 0, v[8:9]
	v_add_u32_e32 v8, 0x60, v24
	v_ashrrev_i32_e32 v9, 31, v8
	v_lshlrev_b64 v[8:9], 14, v[8:9]
	v_lshl_add_u64 v[18:19], v[26:27], 0, v[8:9]
	global_load_dwordx4 v[8:11], v[16:17], off nt
	global_load_dwordx4 v[12:15], v[18:19], off nt
	v_add_u32_e32 v16, 0x80, v24
	v_ashrrev_i32_e32 v17, 31, v16
	v_lshlrev_b64 v[16:17], 14, v[16:17]
	s_waitcnt vmcnt(6)
	v_lshl_add_u64 v[28:29], v[26:27], 0, v[16:17]
	v_add_u32_e32 v16, 0xa0, v24
	v_ashrrev_i32_e32 v17, 31, v16
	v_lshlrev_b64 v[16:17], 14, v[16:17]
	v_lshl_add_u64 v[30:31], v[26:27], 0, v[16:17]
	global_load_dwordx4 v[16:19], v[28:29], off nt
	global_load_dwordx4 v[20:23], v[30:31], off nt
	v_add_u32_e32 v28, 0xc0, v24
	v_ashrrev_i32_e32 v29, 31, v28
	v_add_u32_e32 v24, 0xe0, v24
	v_lshlrev_b64 v[28:29], 14, v[28:29]
	v_ashrrev_i32_e32 v25, 31, v24
	v_lshl_add_u64 v[34:35], v[26:27], 0, v[28:29]
	v_lshlrev_b64 v[24:25], 14, v[24:25]
	v_lshl_add_u64 v[38:39], v[26:27], 0, v[24:25]
	global_load_dwordx4 v[24:27], v[34:35], off nt
	global_load_dwordx4 v[28:31], v[38:39], off nt
	v_add_u32_e32 v39, 0, v32
	v_lshl_add_u64 v[34:35], s[26:27], 0, v[32:33]
	v_lshlrev_b32_e32 v32, 5, v40
	v_ashrrev_i32_e32 v37, 3, v37
	v_and_b32_e32 v32, 0xe0, v32
	s_movk_i32 s2, 0x104
	v_mul_u32_u24_e32 v38, 0x104, v32
	v_lshlrev_b32_e32 v40, 2, v37
	v_add3_u32 v38, 0, v38, v40
	v_mul_lo_u32 v40, v36, s2
	s_lshl_b32 s3, s68, 6
	s_lshl_b32 s2, s46, 6
	v_add_u32_e32 v39, v39, v40
	s_mov_b32 s28, s68
	global_load_dword v200, v[34:35], off
	global_load_dword v200, v[34:35], off
	s_branch .LBB0_46

.LBB0_48:
	s_andn2_b64 vcc, exec, s[10:11]
	s_cbranch_vccnz .LBB0_45
	s_ashr_i32 s10, s26, 31
	s_lshr_b32 s10, s10, 26
	s_add_i32 s10, s26, s10
	s_ashr_i32 s10, s10, 6
	v_lshl_add_u32 v24, s10, 8, v36
	s_add_i32 s27, s2, s3
	s_lshl_b32 s10, s10, 12
	s_sub_i32 s10, s27, s10
	s_ashr_i32 s11, s10, 31
	v_ashrrev_i32_e32 v25, 31, v24
	v_lshl_add_u64 v[26:27], s[10:11], 2, v[34:35]
	v_lshlrev_b64 v[0:1], 14, v[24:25]
	v_lshl_add_u64 v[8:9], v[26:27], 0, v[0:1]
	v_add_u32_e32 v0, 32, v24
	v_ashrrev_i32_e32 v1, 31, v0
	v_lshlrev_b64 v[0:1], 14, v[0:1]
	v_lshl_add_u64 v[10:11], v[26:27], 0, v[0:1]
	global_load_dwordx4 v[0:3], v[8:9], off nt
	global_load_dwordx4 v[4:7], v[10:11], off nt
	v_add_u32_e32 v8, 64, v24
	v_ashrrev_i32_e32 v9, 31, v8
	v_lshlrev_b64 v[8:9], 14, v[8:9]
	v_lshl_add_u64 v[16:17], v[26:27], 0, v[8:9]
	v_add_u32_e32 v8, 0x60, v24
	v_ashrrev_i32_e32 v9, 31, v8
	v_lshlrev_b64 v[8:9], 14, v[8:9]
	v_lshl_add_u64 v[18:19], v[26:27], 0, v[8:9]
	global_load_dwordx4 v[8:11], v[16:17], off nt
	global_load_dwordx4 v[12:15], v[18:19], off nt
	v_add_u32_e32 v16, 0x80, v24
	v_ashrrev_i32_e32 v17, 31, v16
	v_lshlrev_b64 v[16:17], 14, v[16:17]
	v_lshl_add_u64 v[28:29], v[26:27], 0, v[16:17]
	v_add_u32_e32 v16, 0xa0, v24
	v_ashrrev_i32_e32 v17, 31, v16
	v_lshlrev_b64 v[16:17], 14, v[16:17]
	v_lshl_add_u64 v[30:31], v[26:27], 0, v[16:17]
	global_load_dwordx4 v[16:19], v[28:29], off nt
	global_load_dwordx4 v[20:23], v[30:31], off nt
	v_add_u32_e32 v28, 0xc0, v24
	v_ashrrev_i32_e32 v29, 31, v28
	v_add_u32_e32 v24, 0xe0, v24
	v_lshlrev_b64 v[28:29], 14, v[28:29]
	v_ashrrev_i32_e32 v25, 31, v24
	v_lshl_add_u64 v[40:41], v[26:27], 0, v[28:29]
	v_lshlrev_b64 v[24:25], 14, v[24:25]
	v_lshl_add_u64 v[42:43], v[26:27], 0, v[24:25]
	global_load_dwordx4 v[24:27], v[40:41], off nt
	global_load_dwordx4 v[28:31], v[42:43], off nt
	s_branch .LBB0_45

.LBB0_57:
	global_load_dwordx4 v[10:13], v[6:7], off offset:16 nt
	global_load_dwordx4 v[14:17], v[6:7], off nt
	s_waitcnt vmcnt(5)
	v_lshl_add_u64 v[26:27], v[6:7], 0, s[14:15]
	v_lshl_add_u64 v[34:35], v[26:27], 0, s[14:15]
	v_lshl_add_u64 v[42:43], v[34:35], 0, s[14:15]
	global_load_dwordx4 v[18:21], v[26:27], off nt
	global_load_dwordx4 v[22:25], v[26:27], off offset:16 nt
	s_nop 0
	global_load_dwordx4 v[26:29], v[34:35], off nt
	global_load_dwordx4 v[30:33], v[34:35], off offset:16 nt
	s_nop 0
	global_load_dwordx4 v[34:37], v[42:43], off nt
	global_load_dwordx4 v[38:41], v[42:43], off offset:16 nt
	v_lshl_add_u64 v[50:51], v[42:43], 0, s[14:15]
	global_load_dwordx4 v[42:45], v[50:51], off nt
	global_load_dwordx4 v[46:49], v[50:51], off offset:16 nt
	v_lshl_add_u64 v[58:59], v[50:51], 0, s[14:15]
	global_load_dwordx4 v[50:53], v[58:59], off nt
	global_load_dwordx4 v[54:57], v[58:59], off offset:16 nt
	v_lshl_add_u64 v[66:67], v[58:59], 0, s[14:15]
	global_load_dwordx4 v[58:61], v[66:67], off nt
	global_load_dwordx4 v[62:65], v[66:67], off offset:16 nt
	v_lshl_add_u64 v[90:91], v[66:67], 0, s[14:15]
	global_load_dwordx4 v[66:69], v[90:91], off nt
	global_load_dwordx4 v[70:73], v[90:91], off offset:16 nt
	v_mov_b32_e32 v8, 0
	v_mov_b32_e32 v9, 0
	v_mov_b32_e32 v74, 0
	v_mov_b32_e32 v75, 0
	v_mov_b32_e32 v79, 0
	v_mov_b32_e32 v81, 0
	s_add_u32 s0, s4, s4
	v_mov_b32_e32 v78, 0
	v_mov_b32_e32 v80, 0
	v_mov_b32_e32 v82, 0
	v_mov_b32_e32 v83, 0
	s_addc_u32 s1, s5, s5
	v_mov_b32_e32 v84, 0
	v_mov_b32_e32 v85, 0
	s_add_u32 s0, s0, s0
	v_mov_b32_e32 v86, 0
	v_mov_b32_e32 v87, 0
	s_addc_u32 s1, s1, s1
	v_lshl_add_u64 v[76:77], v[4:5], 0, s[26:27]
	v_mov_b32_e32 v88, 0
	v_mov_b32_e32 v89, 0
	s_add_u32 s0, s0, s0
	v_lshl_add_u64 v[90:91], v[76:77], 0, s[26:27]
	s_addc_u32 s1, s1, s1
	v_lshl_add_u64 v[92:93], v[90:91], 0, s[26:27]
	v_lshl_add_u64 v[2:3], s[0:1], 0, v[2:3]
	v_lshl_add_u64 v[94:95], v[92:93], 0, s[26:27]
	v_lshl_add_u64 v[102:103], s[8:9], 0, v[2:3]
	v_lshl_add_u64 v[96:97], v[94:95], 0, s[26:27]
	v_cmp_lt_u64_e32 vcc, s[30:31], v[102:103]
	v_lshl_add_u64 v[6:7], v[6:7], 0, s[12:13]
	v_lshl_add_u64 v[98:99], v[96:97], 0, s[26:27]
	s_or_b64 s[16:17], vcc, s[16:17]
	v_lshl_add_u64 v[100:101], v[98:99], 0, s[26:27]
	s_waitcnt vmcnt(15)
	v_pk_mul_f32 v[10:11], v[10:11], s[28:29] op_sel_hi:[1,0]
	s_waitcnt vmcnt(14)
	v_pk_mul_f32 v[14:15], v[14:15], s[28:29] op_sel_hi:[1,0]
	v_cvt_pk_fp8_f32 v9, v10, v11
	v_cvt_pk_fp8_f32 v8, v14, v15
	s_waitcnt vmcnt(13)
	v_pk_mul_f32 v[14:15], v[18:19], s[28:29] op_sel_hi:[1,0]
	v_pk_mul_f32 v[10:11], v[20:21], s[28:29] op_sel_hi:[1,0]
	s_waitcnt vmcnt(12)
	v_pk_mul_f32 v[18:19], v[24:25], s[28:29] op_sel_hi:[1,0]
	v_pk_mul_f32 v[20:21], v[22:23], s[28:29] op_sel_hi:[1,0]
	v_cvt_pk_fp8_f32 v74, v14, v15
	s_waitcnt vmcnt(11)
	v_pk_mul_f32 v[14:15], v[28:29], s[28:29] op_sel_hi:[1,0]
	s_waitcnt vmcnt(10)
	v_pk_mul_f32 v[24:25], v[30:31], s[28:29] op_sel_hi:[1,0]
	s_waitcnt vmcnt(8)
	v_pk_mul_f32 v[28:29], v[38:39], s[28:29] op_sel_hi:[1,0]
	v_pk_mul_f32 v[16:17], v[16:17], s[28:29] op_sel_hi:[1,0]
	v_cvt_pk_fp8_f32 v75, v20, v21
	v_pk_mul_f32 v[20:21], v[26:27], s[28:29] op_sel_hi:[1,0]
	v_pk_mul_f32 v[22:23], v[32:33], s[28:29] op_sel_hi:[1,0]
	v_cvt_pk_fp8_f32 v79, v24, v25
	v_pk_mul_f32 v[24:25], v[34:35], s[28:29] op_sel_hi:[1,0]
	v_cvt_pk_fp8_f32 v81, v28, v29
	s_waitcnt vmcnt(7)
	v_pk_mul_f32 v[28:29], v[42:43], s[28:29] op_sel_hi:[1,0]
	s_waitcnt vmcnt(6)
	v_pk_mul_f32 v[32:33], v[46:47], s[28:29] op_sel_hi:[1,0]
	v_cvt_pk_fp8_f32 v78, v20, v21
	v_cvt_pk_fp8_f32 v80, v24, v25
	v_cvt_pk_fp8_f32 v8, v16, v17 op_sel:[0,0,1]
	v_cvt_pk_fp8_f32 v82, v28, v29
	v_cvt_pk_fp8_f32 v83, v32, v33
	s_waitcnt vmcnt(5)
	v_pk_mul_f32 v[16:17], v[50:51], s[28:29] op_sel_hi:[1,0]
	s_waitcnt vmcnt(4)
	v_pk_mul_f32 v[32:33], v[54:55], s[28:29] op_sel_hi:[1,0]
	v_cvt_pk_fp8_f32 v84, v16, v17
	v_cvt_pk_fp8_f32 v85, v32, v33
	s_waitcnt vmcnt(3)
	v_pk_mul_f32 v[16:17], v[58:59], s[28:29] op_sel_hi:[1,0]
	s_waitcnt vmcnt(2)
	v_pk_mul_f32 v[32:33], v[62:63], s[28:29] op_sel_hi:[1,0]
	v_pk_mul_f32 v[12:13], v[12:13], s[28:29] op_sel_hi:[1,0]
	v_cvt_pk_fp8_f32 v86, v16, v17
	v_cvt_pk_fp8_f32 v87, v32, v33
	s_waitcnt vmcnt(1)
	v_pk_mul_f32 v[16:17], v[66:67], s[28:29] op_sel_hi:[1,0]
	s_waitcnt vmcnt(0)
	v_pk_mul_f32 v[32:33], v[70:71], s[28:29] op_sel_hi:[1,0]
	v_pk_mul_f32 v[20:21], v[36:37], s[28:29] op_sel_hi:[1,0]
	v_pk_mul_f32 v[26:27], v[40:41], s[28:29] op_sel_hi:[1,0]
	v_pk_mul_f32 v[24:25], v[44:45], s[28:29] op_sel_hi:[1,0]
	v_pk_mul_f32 v[30:31], v[48:49], s[28:29] op_sel_hi:[1,0]
	v_cvt_pk_fp8_f32 v9, v12, v13 op_sel:[0,0,1]
	v_cvt_pk_fp8_f32 v88, v16, v17
	v_cvt_pk_fp8_f32 v89, v32, v33
	v_pk_mul_f32 v[12:13], v[52:53], s[28:29] op_sel_hi:[1,0]
	v_pk_mul_f32 v[28:29], v[56:57], s[28:29] op_sel_hi:[1,0]
	v_cvt_pk_fp8_f32 v74, v10, v11 op_sel:[0,0,1]
	v_cvt_pk_fp8_f32 v75, v18, v19 op_sel:[0,0,1]
	v_cvt_pk_fp8_f32 v78, v14, v15 op_sel:[0,0,1]
	v_cvt_pk_fp8_f32 v79, v22, v23 op_sel:[0,0,1]
	v_cvt_pk_fp8_f32 v80, v20, v21 op_sel:[0,0,1]
	v_cvt_pk_fp8_f32 v81, v26, v27 op_sel:[0,0,1]
	v_cvt_pk_fp8_f32 v82, v24, v25 op_sel:[0,0,1]
	v_cvt_pk_fp8_f32 v83, v30, v31 op_sel:[0,0,1]
	v_pk_mul_f32 v[10:11], v[60:61], s[28:29] op_sel_hi:[1,0]
	v_pk_mul_f32 v[18:19], v[64:65], s[28:29] op_sel_hi:[1,0]
	v_cvt_pk_fp8_f32 v84, v12, v13 op_sel:[0,0,1]
	v_cvt_pk_fp8_f32 v85, v28, v29 op_sel:[0,0,1]
	v_pk_mul_f32 v[14:15], v[68:69], s[28:29] op_sel_hi:[1,0]
	v_pk_mul_f32 v[22:23], v[72:73], s[28:29] op_sel_hi:[1,0]
	v_cvt_pk_fp8_f32 v86, v10, v11 op_sel:[0,0,1]
	v_cvt_pk_fp8_f32 v87, v18, v19 op_sel:[0,0,1]
	global_store_dwordx2 v[4:5], v[8:9], off
	v_lshl_add_u64 v[4:5], v[4:5], 0, s[10:11]
	v_cvt_pk_fp8_f32 v88, v14, v15 op_sel:[0,0,1]
	v_cvt_pk_fp8_f32 v89, v22, v23 op_sel:[0,0,1]
	global_store_dwordx2 v[76:77], v[74:75], off
	global_store_dwordx2 v[90:91], v[78:79], off
	global_store_dwordx2 v[92:93], v[80:81], off
	global_store_dwordx2 v[94:95], v[82:83], off
	global_store_dwordx2 v[96:97], v[84:85], off
	global_store_dwordx2 v[98:99], v[86:87], off
	global_store_dwordx2 v[100:101], v[88:89], off
	s_andn2_b64 exec, exec, s[16:17]
	s_cbranch_execnz .LBB0_57
	s_or_b64 exec, exec, s[16:17]

.LBB0_61:
	global_load_dwordx4 v[8:11], v[4:5], off offset:-16 nt
	global_load_dwordx4 v[12:15], v[4:5], off nt
	s_waitcnt vmcnt(7)
	v_mov_b32_e32 v16, 0
	v_mov_b32_e32 v17, 0
	v_lshl_add_u64 v[2:3], v[2:3], 0, s[4:5]
	v_cmp_lt_u64_e32 vcc, s[16:17], v[2:3]
	v_lshl_add_u64 v[4:5], v[4:5], 0, s[8:9]
	s_or_b64 s[12:13], vcc, s[12:13]
	s_waitcnt vmcnt(1)
	v_pk_mul_f32 v[8:9], v[8:9], s[14:15] op_sel_hi:[1,0]
	s_waitcnt vmcnt(0)
	v_pk_mul_f32 v[12:13], v[12:13], s[14:15] op_sel_hi:[1,0]
	v_cvt_pk_fp8_f32 v16, v8, v9
	v_cvt_pk_fp8_f32 v17, v12, v13
	v_pk_mul_f32 v[10:11], v[10:11], s[14:15] op_sel_hi:[1,0]
	v_pk_mul_f32 v[8:9], v[14:15], s[14:15] op_sel_hi:[1,0]
	v_cvt_pk_fp8_f32 v16, v10, v11 op_sel:[0,0,1]
	v_cvt_pk_fp8_f32 v17, v8, v9 op_sel:[0,0,1]
	global_store_dwordx2 v[6:7], v[16:17], off
	v_lshl_add_u64 v[6:7], v[6:7], 0, s[10:11]
	s_andn2_b64 exec, exec, s[12:13]
	s_cbranch_execnz .LBB0_61
